# P8 residual ladder de-serialised with xb stores deferred past the row-statistics publish; P7 gain loads hoisted out of the row loop
# speedup vs baseline: 1.0017x; 1.0017x over previous
.LBB0_1054:
	s_lshl_b32 s60, s14, 8
	s_add_i32 s63, s63, s60
	v_lshrrev_b32_e32 v130, 2, v185
	v_or_b32_e32 v132, s63, v186
	v_and_b32_e32 v135, 12, v130
	s_lshl_b32 s61, s15, 5
	v_or_b32_e32 v130, s45, v135
	v_ashrrev_i32_e32 v133, 31, v132
	v_or_b32_e32 v140, s61, v130
	v_lshlrev_b64 v[130:131], 13, v[132:133]
	v_lshl_add_u64 v[130:131], s[56:57], 0, v[130:131]
	v_readlane_b32 s6, v246, 3
	v_lshlrev_b32_e32 v162, 1, v140
	v_lshlrev_b32_e32 v134, 2, v140
	v_readlane_b32 s7, v246, 4
	v_lshl_add_u64 v[130:131], v[130:131], 0, v[162:163]
	s_barrier
	v_lshl_add_u32 v244, v132, 13, v162
	global_load_dwordx4 v[220:223], v134, s[6:7]
	global_load_dwordx4 v[224:227], v134, s[6:7] offset:64
	global_load_dwordx4 v[228:231], v134, s[6:7] offset:512
	global_load_dwordx4 v[232:235], v134, s[6:7] offset:576
	global_load_dwordx2 v[188:189], v244, s[56:57]
	global_load_dwordx2 v[190:191], v244, s[56:57] offset:32
	global_load_dwordx2 v[192:193], v244, s[56:57] offset:256
	global_load_dwordx2 v[194:195], v244, s[56:57] offset:288
	v_add_u32_e32 v187, 0x20000, v244
	global_load_dwordx2 v[196:197], v187, s[56:57]
	global_load_dwordx2 v[198:199], v187, s[56:57] offset:32
	global_load_dwordx2 v[200:201], v187, s[56:57] offset:256
	global_load_dwordx2 v[202:203], v187, s[56:57] offset:288
	v_add_u32_e32 v187, 0x40000, v244
	global_load_dwordx2 v[204:205], v187, s[56:57]
	global_load_dwordx2 v[206:207], v187, s[56:57] offset:32
	global_load_dwordx2 v[208:209], v187, s[56:57] offset:256
	global_load_dwordx2 v[210:211], v187, s[56:57] offset:288
	v_add_u32_e32 v187, 0x60000, v244
	global_load_dwordx2 v[212:213], v187, s[56:57]
	global_load_dwordx2 v[214:215], v187, s[56:57] offset:32
	global_load_dwordx2 v[216:217], v187, s[56:57] offset:256
	global_load_dwordx2 v[218:219], v187, s[56:57] offset:288
	v_cvt_f32_i32_e32 v71, v71
	v_cvt_f32_i32_e32 v70, v70
	v_cvt_f32_i32_e32 v73, v73
	v_cvt_f32_i32_e32 v72, v72
	v_cvt_f32_i32_e32 v35, v35
	v_cvt_f32_i32_e32 v34, v34
	v_cvt_f32_i32_e32 v37, v37
	v_cvt_f32_i32_e32 v36, v36
	v_cvt_f32_i32_e32 v19, v19
	v_cvt_f32_i32_e32 v18, v18
	v_cvt_f32_i32_e32 v21, v21
	v_cvt_f32_i32_e32 v20, v20
	v_cvt_f32_i32_e32 v3, v3
	v_cvt_f32_i32_e32 v2, v2
	v_cvt_f32_i32_e32 v5, v5
	v_cvt_f32_i32_e32 v4, v4
	v_cvt_f32_i32_e32 v103, v103
	v_cvt_f32_i32_e32 v102, v102
	v_cvt_f32_i32_e32 v105, v105
	v_cvt_f32_i32_e32 v104, v104
	v_cvt_f32_i32_e32 v55, v55
	v_cvt_f32_i32_e32 v54, v54
	v_cvt_f32_i32_e32 v57, v57
	v_cvt_f32_i32_e32 v56, v56
	v_cvt_f32_i32_e32 v39, v39
	v_cvt_f32_i32_e32 v38, v38
	v_cvt_f32_i32_e32 v41, v41
	v_cvt_f32_i32_e32 v40, v40
	v_cvt_f32_i32_e32 v7, v7
	v_cvt_f32_i32_e32 v6, v6
	v_cvt_f32_i32_e32 v9, v9
	v_cvt_f32_i32_e32 v8, v8
	v_cvt_f32_i32_e32 v115, v115
	v_cvt_f32_i32_e32 v114, v114
	v_cvt_f32_i32_e32 v117, v117
	v_cvt_f32_i32_e32 v116, v116
	v_cvt_f32_i32_e32 v87, v87
	v_cvt_f32_i32_e32 v86, v86
	v_cvt_f32_i32_e32 v89, v89
	v_cvt_f32_i32_e32 v88, v88
	v_cvt_f32_i32_e32 v67, v67
	v_cvt_f32_i32_e32 v66, v66
	v_cvt_f32_i32_e32 v69, v69
	v_cvt_f32_i32_e32 v68, v68
	v_cvt_f32_i32_e32 v27, v27
	v_cvt_f32_i32_e32 v26, v26
	v_cvt_f32_i32_e32 v29, v29
	v_cvt_f32_i32_e32 v28, v28
	v_cvt_f32_i32_e32 v127, v127
	v_cvt_f32_i32_e32 v126, v126
	v_cvt_f32_i32_e32 v129, v129
	v_cvt_f32_i32_e32 v128, v128
	v_cvt_f32_i32_e32 v111, v111
	v_cvt_f32_i32_e32 v110, v110
	v_cvt_f32_i32_e32 v113, v113
	v_cvt_f32_i32_e32 v112, v112
	v_cvt_f32_i32_e32 v91, v91
	v_cvt_f32_i32_e32 v90, v90
	v_cvt_f32_i32_e32 v93, v93
	v_cvt_f32_i32_e32 v92, v92
	v_cvt_f32_i32_e32 v51, v51
	v_cvt_f32_i32_e32 v50, v50
	v_cvt_f32_i32_e32 v53, v53
	v_cvt_f32_i32_e32 v52, v52
	v_cvt_f32_i32_e32 v123, v123
	v_cvt_f32_i32_e32 v122, v122
	v_cvt_f32_i32_e32 v125, v125
	v_cvt_f32_i32_e32 v124, v124
	v_cvt_f32_i32_e32 v119, v119
	v_cvt_f32_i32_e32 v118, v118
	v_cvt_f32_i32_e32 v121, v121
	v_cvt_f32_i32_e32 v120, v120
	v_cvt_f32_i32_e32 v107, v107
	v_cvt_f32_i32_e32 v106, v106
	v_cvt_f32_i32_e32 v109, v109
	v_cvt_f32_i32_e32 v108, v108
	v_cvt_f32_i32_e32 v83, v83
	v_cvt_f32_i32_e32 v82, v82
	v_cvt_f32_i32_e32 v85, v85
	v_cvt_f32_i32_e32 v84, v84
	v_cvt_f32_i32_e32 v99, v99
	v_cvt_f32_i32_e32 v98, v98
	v_cvt_f32_i32_e32 v101, v101
	v_cvt_f32_i32_e32 v100, v100
	v_cvt_f32_i32_e32 v95, v95
	v_cvt_f32_i32_e32 v94, v94
	v_cvt_f32_i32_e32 v97, v97
	v_cvt_f32_i32_e32 v96, v96
	v_cvt_f32_i32_e32 v79, v79
	v_cvt_f32_i32_e32 v78, v78
	v_cvt_f32_i32_e32 v81, v81
	v_cvt_f32_i32_e32 v80, v80
	v_cvt_f32_i32_e32 v75, v75
	v_cvt_f32_i32_e32 v74, v74
	v_cvt_f32_i32_e32 v77, v77
	v_cvt_f32_i32_e32 v76, v76
	v_cvt_f32_i32_e32 v63, v63
	v_cvt_f32_i32_e32 v62, v62
	v_cvt_f32_i32_e32 v65, v65
	v_cvt_f32_i32_e32 v64, v64
	v_cvt_f32_i32_e32 v59, v59
	v_cvt_f32_i32_e32 v58, v58
	v_cvt_f32_i32_e32 v61, v61
	v_cvt_f32_i32_e32 v60, v60
	v_cvt_f32_i32_e32 v47, v47
	v_cvt_f32_i32_e32 v46, v46
	v_cvt_f32_i32_e32 v49, v49
	v_cvt_f32_i32_e32 v48, v48
	v_cvt_f32_i32_e32 v43, v43
	v_cvt_f32_i32_e32 v42, v42
	v_cvt_f32_i32_e32 v45, v45
	v_cvt_f32_i32_e32 v44, v44
	v_cvt_f32_i32_e32 v31, v31
	v_cvt_f32_i32_e32 v30, v30
	v_cvt_f32_i32_e32 v33, v33
	v_cvt_f32_i32_e32 v32, v32
	v_cvt_f32_i32_e32 v23, v23
	v_cvt_f32_i32_e32 v22, v22
	v_cvt_f32_i32_e32 v25, v25
	v_cvt_f32_i32_e32 v24, v24
	v_cvt_f32_i32_e32 v15, v15
	v_cvt_f32_i32_e32 v14, v14
	v_cvt_f32_i32_e32 v17, v17
	v_cvt_f32_i32_e32 v16, v16
	v_cvt_f32_i32_e32 v11, v11
	v_cvt_f32_i32_e32 v10, v10
	v_cvt_f32_i32_e32 v13, v13
	v_cvt_f32_i32_e32 v12, v12
	s_waitcnt vmcnt(16)
	v_pk_mul_f32 v[220:221], v[220:221], s[38:39] op_sel_hi:[1,0]
	v_pk_mul_f32 v[222:223], v[222:223], s[38:39] op_sel_hi:[1,0]
	v_pk_mul_f32 v[224:225], v[224:225], s[38:39] op_sel_hi:[1,0]
	v_pk_mul_f32 v[226:227], v[226:227], s[38:39] op_sel_hi:[1,0]
	v_pk_mul_f32 v[228:229], v[228:229], s[38:39] op_sel_hi:[1,0]
	v_pk_mul_f32 v[230:231], v[230:231], s[38:39] op_sel_hi:[1,0]
	v_pk_mul_f32 v[232:233], v[232:233], s[38:39] op_sel_hi:[1,0]
	v_pk_mul_f32 v[234:235], v[234:235], s[38:39] op_sel_hi:[1,0]
	s_waitcnt vmcnt(14)
	v_lshlrev_b32_e32 v236, 16, v188
	v_and_b32_e32 v237, 0xffff0000, v188
	v_lshlrev_b32_e32 v238, 16, v189
	v_and_b32_e32 v239, 0xffff0000, v189
	v_lshlrev_b32_e32 v240, 16, v190
	v_and_b32_e32 v241, 0xffff0000, v190
	v_lshlrev_b32_e32 v242, 16, v191
	v_and_b32_e32 v243, 0xffff0000, v191
	v_pk_fma_f32 v[72:73], v[222:223], v[72:73], v[238:239]
	v_pk_fma_f32 v[70:71], v[220:221], v[70:71], v[236:237]
	v_pk_fma_f32 v[36:37], v[226:227], v[36:37], v[242:243]
	v_pk_fma_f32 v[34:35], v[224:225], v[34:35], v[240:241]
	v_add_u32_e32 v187, 0x100000, v244
	global_load_dwordx2 v[188:189], v187, s[56:57]
	global_load_dwordx2 v[190:191], v187, s[56:57] offset:32
	s_waitcnt vmcnt(14)
	v_lshlrev_b32_e32 v236, 16, v192
	v_and_b32_e32 v237, 0xffff0000, v192
	v_lshlrev_b32_e32 v238, 16, v193
	v_and_b32_e32 v239, 0xffff0000, v193
	v_lshlrev_b32_e32 v240, 16, v194
	v_and_b32_e32 v241, 0xffff0000, v194
	v_lshlrev_b32_e32 v242, 16, v195
	v_and_b32_e32 v243, 0xffff0000, v195
	v_pk_fma_f32 v[20:21], v[230:231], v[20:21], v[238:239]
	v_pk_fma_f32 v[18:19], v[228:229], v[18:19], v[236:237]
	v_pk_fma_f32 v[4:5], v[234:235], v[4:5], v[242:243]
	v_pk_fma_f32 v[2:3], v[232:233], v[2:3], v[240:241]
	global_load_dwordx2 v[192:193], v187, s[56:57] offset:256
	global_load_dwordx2 v[194:195], v187, s[56:57] offset:288
	s_waitcnt vmcnt(14)
	v_lshlrev_b32_e32 v236, 16, v196
	v_and_b32_e32 v237, 0xffff0000, v196
	v_lshlrev_b32_e32 v238, 16, v197
	v_and_b32_e32 v239, 0xffff0000, v197
	v_lshlrev_b32_e32 v240, 16, v198
	v_and_b32_e32 v241, 0xffff0000, v198
	v_lshlrev_b32_e32 v242, 16, v199
	v_and_b32_e32 v243, 0xffff0000, v199
	v_pk_fma_f32 v[104:105], v[222:223], v[104:105], v[238:239]
	v_pk_fma_f32 v[102:103], v[220:221], v[102:103], v[236:237]
	v_pk_fma_f32 v[56:57], v[226:227], v[56:57], v[242:243]
	v_pk_fma_f32 v[54:55], v[224:225], v[54:55], v[240:241]
	v_add_u32_e32 v187, 0x120000, v244
	global_load_dwordx2 v[196:197], v187, s[56:57]
	global_load_dwordx2 v[198:199], v187, s[56:57] offset:32
	s_waitcnt vmcnt(14)
	v_lshlrev_b32_e32 v236, 16, v200
	v_and_b32_e32 v237, 0xffff0000, v200
	v_lshlrev_b32_e32 v238, 16, v201
	v_and_b32_e32 v239, 0xffff0000, v201
	v_lshlrev_b32_e32 v240, 16, v202
	v_and_b32_e32 v241, 0xffff0000, v202
	v_lshlrev_b32_e32 v242, 16, v203
	v_and_b32_e32 v243, 0xffff0000, v203
	v_pk_fma_f32 v[40:41], v[230:231], v[40:41], v[238:239]
	v_pk_fma_f32 v[38:39], v[228:229], v[38:39], v[236:237]
	v_pk_fma_f32 v[8:9], v[234:235], v[8:9], v[242:243]
	v_pk_fma_f32 v[6:7], v[232:233], v[6:7], v[240:241]
	global_load_dwordx2 v[200:201], v187, s[56:57] offset:256
	global_load_dwordx2 v[202:203], v187, s[56:57] offset:288
	s_waitcnt vmcnt(14)
	v_lshlrev_b32_e32 v236, 16, v204
	v_and_b32_e32 v237, 0xffff0000, v204
	v_lshlrev_b32_e32 v238, 16, v205
	v_and_b32_e32 v239, 0xffff0000, v205
	v_lshlrev_b32_e32 v240, 16, v206
	v_and_b32_e32 v241, 0xffff0000, v206
	v_lshlrev_b32_e32 v242, 16, v207
	v_and_b32_e32 v243, 0xffff0000, v207
	v_pk_fma_f32 v[116:117], v[222:223], v[116:117], v[238:239]
	v_pk_fma_f32 v[114:115], v[220:221], v[114:115], v[236:237]
	v_pk_fma_f32 v[88:89], v[226:227], v[88:89], v[242:243]
	v_pk_fma_f32 v[86:87], v[224:225], v[86:87], v[240:241]
	v_add_u32_e32 v187, 0x140000, v244
	global_load_dwordx2 v[204:205], v187, s[56:57]
	global_load_dwordx2 v[206:207], v187, s[56:57] offset:32
	s_waitcnt vmcnt(14)
	v_lshlrev_b32_e32 v236, 16, v208
	v_and_b32_e32 v237, 0xffff0000, v208
	v_lshlrev_b32_e32 v238, 16, v209
	v_and_b32_e32 v239, 0xffff0000, v209
	v_lshlrev_b32_e32 v240, 16, v210
	v_and_b32_e32 v241, 0xffff0000, v210
	v_lshlrev_b32_e32 v242, 16, v211
	v_and_b32_e32 v243, 0xffff0000, v211
	v_pk_fma_f32 v[68:69], v[230:231], v[68:69], v[238:239]
	v_pk_fma_f32 v[66:67], v[228:229], v[66:67], v[236:237]
	v_pk_fma_f32 v[28:29], v[234:235], v[28:29], v[242:243]
	v_pk_fma_f32 v[26:27], v[232:233], v[26:27], v[240:241]
	global_load_dwordx2 v[208:209], v187, s[56:57] offset:256
	global_load_dwordx2 v[210:211], v187, s[56:57] offset:288
	s_waitcnt vmcnt(14)
	v_lshlrev_b32_e32 v236, 16, v212
	v_and_b32_e32 v237, 0xffff0000, v212
	v_lshlrev_b32_e32 v238, 16, v213
	v_and_b32_e32 v239, 0xffff0000, v213
	v_lshlrev_b32_e32 v240, 16, v214
	v_and_b32_e32 v241, 0xffff0000, v214
	v_lshlrev_b32_e32 v242, 16, v215
	v_and_b32_e32 v243, 0xffff0000, v215
	v_pk_fma_f32 v[128:129], v[222:223], v[128:129], v[238:239]
	v_pk_fma_f32 v[126:127], v[220:221], v[126:127], v[236:237]
	v_pk_fma_f32 v[112:113], v[226:227], v[112:113], v[242:243]
	v_pk_fma_f32 v[110:111], v[224:225], v[110:111], v[240:241]
	v_add_u32_e32 v187, 0x160000, v244
	global_load_dwordx2 v[212:213], v187, s[56:57]
	global_load_dwordx2 v[214:215], v187, s[56:57] offset:32
	s_waitcnt vmcnt(14)
	v_lshlrev_b32_e32 v236, 16, v216
	v_and_b32_e32 v237, 0xffff0000, v216
	v_lshlrev_b32_e32 v238, 16, v217
	v_and_b32_e32 v239, 0xffff0000, v217
	v_lshlrev_b32_e32 v240, 16, v218
	v_and_b32_e32 v241, 0xffff0000, v218
	v_lshlrev_b32_e32 v242, 16, v219
	v_and_b32_e32 v243, 0xffff0000, v219
	v_pk_fma_f32 v[92:93], v[230:231], v[92:93], v[238:239]
	v_pk_fma_f32 v[90:91], v[228:229], v[90:91], v[236:237]
	v_pk_fma_f32 v[52:53], v[234:235], v[52:53], v[242:243]
	v_pk_fma_f32 v[50:51], v[232:233], v[50:51], v[240:241]
	global_load_dwordx2 v[216:217], v187, s[56:57] offset:256
	global_load_dwordx2 v[218:219], v187, s[56:57] offset:288
	s_waitcnt vmcnt(14)
	v_lshlrev_b32_e32 v236, 16, v188
	v_and_b32_e32 v237, 0xffff0000, v188
	v_lshlrev_b32_e32 v238, 16, v189
	v_and_b32_e32 v239, 0xffff0000, v189
	v_lshlrev_b32_e32 v240, 16, v190
	v_and_b32_e32 v241, 0xffff0000, v190
	v_lshlrev_b32_e32 v242, 16, v191
	v_and_b32_e32 v243, 0xffff0000, v191
	v_pk_fma_f32 v[124:125], v[222:223], v[124:125], v[238:239]
	v_pk_fma_f32 v[122:123], v[220:221], v[122:123], v[236:237]
	v_pk_fma_f32 v[120:121], v[226:227], v[120:121], v[242:243]
	v_pk_fma_f32 v[118:119], v[224:225], v[118:119], v[240:241]
	s_waitcnt vmcnt(12)
	v_lshlrev_b32_e32 v236, 16, v192
	v_and_b32_e32 v237, 0xffff0000, v192
	v_lshlrev_b32_e32 v238, 16, v193
	v_and_b32_e32 v239, 0xffff0000, v193
	v_lshlrev_b32_e32 v240, 16, v194
	v_and_b32_e32 v241, 0xffff0000, v194
	v_lshlrev_b32_e32 v242, 16, v195
	v_and_b32_e32 v243, 0xffff0000, v195
	v_pk_fma_f32 v[108:109], v[230:231], v[108:109], v[238:239]
	v_pk_fma_f32 v[106:107], v[228:229], v[106:107], v[236:237]
	v_pk_fma_f32 v[84:85], v[234:235], v[84:85], v[242:243]
	v_pk_fma_f32 v[82:83], v[232:233], v[82:83], v[240:241]
	s_waitcnt vmcnt(10)
	v_lshlrev_b32_e32 v236, 16, v196
	v_and_b32_e32 v237, 0xffff0000, v196
	v_lshlrev_b32_e32 v238, 16, v197
	v_and_b32_e32 v239, 0xffff0000, v197
	v_lshlrev_b32_e32 v240, 16, v198
	v_and_b32_e32 v241, 0xffff0000, v198
	v_lshlrev_b32_e32 v242, 16, v199
	v_and_b32_e32 v243, 0xffff0000, v199
	v_pk_fma_f32 v[100:101], v[222:223], v[100:101], v[238:239]
	v_pk_fma_f32 v[98:99], v[220:221], v[98:99], v[236:237]
	v_pk_fma_f32 v[96:97], v[226:227], v[96:97], v[242:243]
	v_pk_fma_f32 v[94:95], v[224:225], v[94:95], v[240:241]
	s_waitcnt vmcnt(8)
	v_lshlrev_b32_e32 v236, 16, v200
	v_and_b32_e32 v237, 0xffff0000, v200
	v_lshlrev_b32_e32 v238, 16, v201
	v_and_b32_e32 v239, 0xffff0000, v201
	v_lshlrev_b32_e32 v240, 16, v202
	v_and_b32_e32 v241, 0xffff0000, v202
	v_lshlrev_b32_e32 v242, 16, v203
	v_and_b32_e32 v243, 0xffff0000, v203
	v_pk_fma_f32 v[80:81], v[230:231], v[80:81], v[238:239]
	v_pk_fma_f32 v[78:79], v[228:229], v[78:79], v[236:237]
	v_pk_fma_f32 v[76:77], v[234:235], v[76:77], v[242:243]
	v_pk_fma_f32 v[74:75], v[232:233], v[74:75], v[240:241]
	s_waitcnt vmcnt(6)
	v_lshlrev_b32_e32 v236, 16, v204
	v_and_b32_e32 v237, 0xffff0000, v204
	v_lshlrev_b32_e32 v238, 16, v205
	v_and_b32_e32 v239, 0xffff0000, v205
	v_lshlrev_b32_e32 v240, 16, v206
	v_and_b32_e32 v241, 0xffff0000, v206
	v_lshlrev_b32_e32 v242, 16, v207
	v_and_b32_e32 v243, 0xffff0000, v207
	v_pk_fma_f32 v[64:65], v[222:223], v[64:65], v[238:239]
	v_pk_fma_f32 v[62:63], v[220:221], v[62:63], v[236:237]
	v_pk_fma_f32 v[60:61], v[226:227], v[60:61], v[242:243]
	v_pk_fma_f32 v[58:59], v[224:225], v[58:59], v[240:241]
	s_waitcnt vmcnt(4)
	v_lshlrev_b32_e32 v236, 16, v208
	v_and_b32_e32 v237, 0xffff0000, v208
	v_lshlrev_b32_e32 v238, 16, v209
	v_and_b32_e32 v239, 0xffff0000, v209
	v_lshlrev_b32_e32 v240, 16, v210
	v_and_b32_e32 v241, 0xffff0000, v210
	v_lshlrev_b32_e32 v242, 16, v211
	v_and_b32_e32 v243, 0xffff0000, v211
	v_pk_fma_f32 v[48:49], v[230:231], v[48:49], v[238:239]
	v_pk_fma_f32 v[46:47], v[228:229], v[46:47], v[236:237]
	v_pk_fma_f32 v[44:45], v[234:235], v[44:45], v[242:243]
	v_pk_fma_f32 v[42:43], v[232:233], v[42:43], v[240:241]
	s_waitcnt vmcnt(2)
	v_lshlrev_b32_e32 v236, 16, v212
	v_and_b32_e32 v237, 0xffff0000, v212
	v_lshlrev_b32_e32 v238, 16, v213
	v_and_b32_e32 v239, 0xffff0000, v213
	v_lshlrev_b32_e32 v240, 16, v214
	v_and_b32_e32 v241, 0xffff0000, v214
	v_lshlrev_b32_e32 v242, 16, v215
	v_and_b32_e32 v243, 0xffff0000, v215
	v_pk_fma_f32 v[32:33], v[222:223], v[32:33], v[238:239]
	v_pk_fma_f32 v[30:31], v[220:221], v[30:31], v[236:237]
	v_pk_fma_f32 v[24:25], v[226:227], v[24:25], v[242:243]
	v_pk_fma_f32 v[22:23], v[224:225], v[22:23], v[240:241]
	s_waitcnt vmcnt(0)
	v_lshlrev_b32_e32 v236, 16, v216
	v_and_b32_e32 v237, 0xffff0000, v216
	v_lshlrev_b32_e32 v238, 16, v217
	v_and_b32_e32 v239, 0xffff0000, v217
	v_lshlrev_b32_e32 v240, 16, v218
	v_and_b32_e32 v241, 0xffff0000, v218
	v_lshlrev_b32_e32 v242, 16, v219
	v_and_b32_e32 v243, 0xffff0000, v219
	v_pk_fma_f32 v[16:17], v[230:231], v[16:17], v[238:239]
	v_pk_fma_f32 v[14:15], v[228:229], v[14:15], v[236:237]
	v_pk_fma_f32 v[12:13], v[234:235], v[12:13], v[242:243]
	v_pk_fma_f32 v[10:11], v[232:233], v[10:11], v[240:241]
	s_lshl_b32 s4, s15, 2
	v_mul_f32_e32 v152, v37, v37
	v_fmac_f32_e32 v152, v36, v36
	v_mul_f32_e32 v153, v5, v5
	v_fmac_f32_e32 v153, v4, v4
	v_mul_f32_e32 v138, v73, v73
	v_mul_f32_e32 v136, v71, v71
	v_mul_f32_e32 v139, v35, v35
	v_fmac_f32_e32 v136, v70, v70
	v_fmac_f32_e32 v138, v72, v72
	v_fmac_f32_e32 v139, v34, v34
	v_add_f32_e32 v136, v136, v138
	v_add_f32_e32 v138, v139, v152
	v_and_b32_e32 v133, 64, v1
	v_add_f32_e32 v136, v136, v138
	v_mul_f32_e32 v138, v19, v19
	v_mul_f32_e32 v139, v21, v21
	v_xor_b32_e32 v132, 16, v1
	v_add_u32_e32 v133, 64, v133
	v_mul_f32_e32 v152, v3, v3
	v_fmac_f32_e32 v138, v18, v18
	v_fmac_f32_e32 v139, v20, v20
	v_cmp_lt_i32_e32 vcc, v132, v133
	v_fmac_f32_e32 v152, v2, v2
	v_add_f32_e32 v138, v138, v139
	v_cndmask_b32_e32 v132, v1, v132, vcc
	v_add_f32_e32 v139, v152, v153
	v_add_f32_e32 v136, v136, v138
	v_lshlrev_b32_e32 v132, 2, v132
	v_add_f32_e32 v136, v139, v136
	ds_bpermute_b32 v138, v132, v136
	v_xor_b32_e32 v139, 32, v1
	v_cmp_lt_i32_e32 vcc, v139, v133
	v_and_b32_e32 v137, 63, v185
	s_add_i32 s6, s4, 0
	v_cndmask_b32_e32 v133, v1, v139, vcc
	v_lshlrev_b32_e32 v133, 2, v133
	s_waitcnt lgkmcnt(0)
	v_add_f32_e32 v136, v136, v138
	ds_bpermute_b32 v138, v133, v136
	v_cmp_gt_u32_e32 vcc, 16, v137
	s_and_saveexec_b64 s[4:5], vcc
	s_cbranch_execz .LBB0_1056
	s_lshl_b32 s7, s19, 10
	s_add_i32 s7, s6, s7
	v_lshl_add_u32 v130, v186, 4, s7
	s_waitcnt lgkmcnt(0)
	v_add_f32_e32 v131, v136, v138
	ds_write_b32 v130, v131

.LBB0_1075:
	s_or_b64 exec, exec, s[18:19]
	v_cvt_pk_bf16_f32 v236, v70, v71
	v_cvt_pk_bf16_f32 v237, v72, v73
	v_cvt_pk_bf16_f32 v238, v34, v35
	v_cvt_pk_bf16_f32 v239, v36, v37
	global_store_dwordx2 v244, v[236:237], s[56:57]
	global_store_dwordx2 v244, v[238:239], s[56:57] offset:32
	v_cvt_pk_bf16_f32 v240, v18, v19
	v_cvt_pk_bf16_f32 v241, v20, v21
	v_cvt_pk_bf16_f32 v242, v2, v3
	v_cvt_pk_bf16_f32 v243, v4, v5
	global_store_dwordx2 v244, v[240:241], s[56:57] offset:256
	global_store_dwordx2 v244, v[242:243], s[56:57] offset:288
	v_add_u32_e32 v245, 0x20000, v244
	v_cvt_pk_bf16_f32 v236, v102, v103
	v_cvt_pk_bf16_f32 v237, v104, v105
	v_cvt_pk_bf16_f32 v238, v54, v55
	v_cvt_pk_bf16_f32 v239, v56, v57
	global_store_dwordx2 v245, v[236:237], s[56:57]
	global_store_dwordx2 v245, v[238:239], s[56:57] offset:32
	v_cvt_pk_bf16_f32 v240, v38, v39
	v_cvt_pk_bf16_f32 v241, v40, v41
	v_cvt_pk_bf16_f32 v242, v6, v7
	v_cvt_pk_bf16_f32 v243, v8, v9
	global_store_dwordx2 v245, v[240:241], s[56:57] offset:256
	global_store_dwordx2 v245, v[242:243], s[56:57] offset:288
	v_add_u32_e32 v245, 0x40000, v244
	v_cvt_pk_bf16_f32 v236, v114, v115
	v_cvt_pk_bf16_f32 v237, v116, v117
	v_cvt_pk_bf16_f32 v238, v86, v87
	v_cvt_pk_bf16_f32 v239, v88, v89
	global_store_dwordx2 v245, v[236:237], s[56:57]
	global_store_dwordx2 v245, v[238:239], s[56:57] offset:32
	v_cvt_pk_bf16_f32 v240, v66, v67
	v_cvt_pk_bf16_f32 v241, v68, v69
	v_cvt_pk_bf16_f32 v242, v26, v27
	v_cvt_pk_bf16_f32 v243, v28, v29
	global_store_dwordx2 v245, v[240:241], s[56:57] offset:256
	global_store_dwordx2 v245, v[242:243], s[56:57] offset:288
	v_add_u32_e32 v245, 0x60000, v244
	v_cvt_pk_bf16_f32 v236, v126, v127
	v_cvt_pk_bf16_f32 v237, v128, v129
	v_cvt_pk_bf16_f32 v238, v110, v111
	v_cvt_pk_bf16_f32 v239, v112, v113
	global_store_dwordx2 v245, v[236:237], s[56:57]
	global_store_dwordx2 v245, v[238:239], s[56:57] offset:32
	v_cvt_pk_bf16_f32 v240, v90, v91
	v_cvt_pk_bf16_f32 v241, v92, v93
	v_cvt_pk_bf16_f32 v242, v50, v51
	v_cvt_pk_bf16_f32 v243, v52, v53
	global_store_dwordx2 v245, v[240:241], s[56:57] offset:256
	global_store_dwordx2 v245, v[242:243], s[56:57] offset:288
	v_add_u32_e32 v245, 0x100000, v244
	v_cvt_pk_bf16_f32 v236, v122, v123
	v_cvt_pk_bf16_f32 v237, v124, v125
	v_cvt_pk_bf16_f32 v238, v118, v119
	v_cvt_pk_bf16_f32 v239, v120, v121
	global_store_dwordx2 v245, v[236:237], s[56:57]
	global_store_dwordx2 v245, v[238:239], s[56:57] offset:32
	v_cvt_pk_bf16_f32 v240, v106, v107
	v_cvt_pk_bf16_f32 v241, v108, v109
	v_cvt_pk_bf16_f32 v242, v82, v83
	v_cvt_pk_bf16_f32 v243, v84, v85
	global_store_dwordx2 v245, v[240:241], s[56:57] offset:256
	global_store_dwordx2 v245, v[242:243], s[56:57] offset:288
	v_add_u32_e32 v245, 0x120000, v244
	v_cvt_pk_bf16_f32 v236, v98, v99
	v_cvt_pk_bf16_f32 v237, v100, v101
	v_cvt_pk_bf16_f32 v238, v94, v95
	v_cvt_pk_bf16_f32 v239, v96, v97
	global_store_dwordx2 v245, v[236:237], s[56:57]
	global_store_dwordx2 v245, v[238:239], s[56:57] offset:32
	v_cvt_pk_bf16_f32 v240, v78, v79
	v_cvt_pk_bf16_f32 v241, v80, v81
	v_cvt_pk_bf16_f32 v242, v74, v75
	v_cvt_pk_bf16_f32 v243, v76, v77
	global_store_dwordx2 v245, v[240:241], s[56:57] offset:256
	global_store_dwordx2 v245, v[242:243], s[56:57] offset:288
	v_add_u32_e32 v245, 0x140000, v244
	v_cvt_pk_bf16_f32 v236, v62, v63
	v_cvt_pk_bf16_f32 v237, v64, v65
	v_cvt_pk_bf16_f32 v238, v58, v59
	v_cvt_pk_bf16_f32 v239, v60, v61
	global_store_dwordx2 v245, v[236:237], s[56:57]
	global_store_dwordx2 v245, v[238:239], s[56:57] offset:32
	v_cvt_pk_bf16_f32 v240, v46, v47
	v_cvt_pk_bf16_f32 v241, v48, v49
	v_cvt_pk_bf16_f32 v242, v42, v43
	v_cvt_pk_bf16_f32 v243, v44, v45
	global_store_dwordx2 v245, v[240:241], s[56:57] offset:256
	global_store_dwordx2 v245, v[242:243], s[56:57] offset:288
	v_add_u32_e32 v245, 0x160000, v244
	v_cvt_pk_bf16_f32 v236, v30, v31
	v_cvt_pk_bf16_f32 v237, v32, v33
	v_cvt_pk_bf16_f32 v238, v22, v23
	v_cvt_pk_bf16_f32 v239, v24, v25
	global_store_dwordx2 v245, v[236:237], s[56:57]
	global_store_dwordx2 v245, v[238:239], s[56:57] offset:32
	v_cvt_pk_bf16_f32 v240, v14, v15
	v_cvt_pk_bf16_f32 v241, v16, v17
	v_cvt_pk_bf16_f32 v242, v10, v11
	v_cvt_pk_bf16_f32 v243, v12, v13
	global_store_dwordx2 v245, v[240:241], s[56:57] offset:256
	global_store_dwordx2 v245, v[242:243], s[56:57] offset:288
	s_cmp_gt_u32 s59, 63
	s_cbranch_scc1 .LBB0_1092
	s_memrealtime s[18:19]
	s_lshl_b32 s14, s14, 6
	s_ashr_i32 s15, s14, 31
	s_lshl_b64 s[14:15], s[14:15], 2
	s_add_u32 s14, s3, s14
	s_addc_u32 s15, s39, s15
	s_branch .LBB0_1079

	.amdhsa_kernel _Z9hymba_fwd4Args
		.amdhsa_group_segment_fixed_size 0
		.amdhsa_private_segment_fixed_size 0
		.amdhsa_kernarg_size 480
		.amdhsa_user_sgpr_count 2
		.amdhsa_user_sgpr_dispatch_ptr 0
		.amdhsa_user_sgpr_queue_ptr 0
		.amdhsa_user_sgpr_kernarg_segment_ptr 1
		.amdhsa_user_sgpr_dispatch_id 0
		.amdhsa_user_sgpr_kernarg_preload_length 0
		.amdhsa_user_sgpr_kernarg_preload_offset 0
		.amdhsa_user_sgpr_private_segment_size 0
		.amdhsa_uses_dynamic_stack 0
		.amdhsa_enable_private_segment 0
		.amdhsa_system_sgpr_workgroup_id_x 1
		.amdhsa_system_sgpr_workgroup_id_y 0
		.amdhsa_system_sgpr_workgroup_id_z 0
		.amdhsa_system_sgpr_workgroup_info 0
		.amdhsa_system_vgpr_workitem_id 0
		.amdhsa_next_free_vgpr 248
		.amdhsa_next_free_sgpr 102
		.amdhsa_accum_offset 248
		.amdhsa_reserve_vcc 1
		.amdhsa_float_round_mode_32 0
		.amdhsa_float_round_mode_16_64 0
		.amdhsa_float_denorm_mode_32 3
		.amdhsa_float_denorm_mode_16_64 3
		.amdhsa_dx10_clamp 1
		.amdhsa_ieee_mode 1
		.amdhsa_fp16_overflow 0
		.amdhsa_tg_split 0
		.amdhsa_exception_fp_ieee_invalid_op 0
		.amdhsa_exception_fp_denorm_src 0
		.amdhsa_exception_fp_ieee_div_zero 0
		.amdhsa_exception_fp_ieee_overflow 0
		.amdhsa_exception_fp_ieee_underflow 0
		.amdhsa_exception_fp_ieee_inexact 0
		.amdhsa_exception_int_div_zero 0
	.end_amdhsa_kernel

amdhsa.kernels:
  - .agpr_count:     0
    .args:
      - .offset:         0
        .size:           224
        .value_kind:     by_value
      - .offset:         224
        .size:           4
        .value_kind:     hidden_block_count_x
      - .offset:         228
        .size:           4
        .value_kind:     hidden_block_count_y
      - .offset:         232
        .size:           4
        .value_kind:     hidden_block_count_z
      - .offset:         236
        .size:           2
        .value_kind:     hidden_group_size_x
      - .offset:         238
        .size:           2
        .value_kind:     hidden_group_size_y
      - .offset:         240
        .size:           2
        .value_kind:     hidden_group_size_z
      - .offset:         242
        .size:           2
        .value_kind:     hidden_remainder_x
      - .offset:         244
        .size:           2
        .value_kind:     hidden_remainder_y
      - .offset:         246
        .size:           2
        .value_kind:     hidden_remainder_z
      - .offset:         264
        .size:           8
        .value_kind:     hidden_global_offset_x
      - .offset:         272
        .size:           8
        .value_kind:     hidden_global_offset_y
      - .offset:         280
        .size:           8
        .value_kind:     hidden_global_offset_z
      - .offset:         288
        .size:           2
        .value_kind:     hidden_grid_dims
      - .offset:         344
        .size:           4
        .value_kind:     hidden_dynamic_lds_size
    .group_segment_fixed_size: 0
    .kernarg_segment_align: 8
    .kernarg_segment_size: 480
    .language:       OpenCL C
    .language_version:
      - 2
      - 0
    .max_flat_workgroup_size: 512
    .name:           _Z9hymba_fwd4Args
    .private_segment_fixed_size: 0
    .sgpr_count:     108
    .sgpr_spill_count: 127
    .symbol:         _Z9hymba_fwd4Args.kd
    .uniform_work_group_size: 1
    .uses_dynamic_stack: false
    .vgpr_count:     248
    .vgpr_spill_count: 0
    .wavefront_size: 64
